# speedup vs baseline: 1.0035x; 1.0029x over previous
.LBB1_3:
	s_mov_b32 s29, s16
	v_add_u32_e32 v0, s29, v101
	ds_read_b128 v[94:97], v0 offset:16384
	ds_read_b128 v[102:105], v0 offset:17408
	ds_read_b128 v[106:109], v0 offset:18432
	ds_read_b128 v[110:113], v0 offset:19456
	ds_read_b128 v[114:117], v0 offset:32768
	ds_read_b128 v[118:121], v0 offset:33792
	ds_read_b128 v[122:125], v0 offset:34816
	ds_read_b128 v[126:129], v0 offset:35840
	s_lshl_b32 s16, s28, 2
	s_or_b32 s16, s16, s23
	s_lshl_b64 s[30:31], s[16:17], 19
	s_add_u32 s16, s6, s30
	s_addc_u32 s31, s7, s31
	s_lshl_b32 s33, s3, 7
	s_ashr_i32 s35, s33, 31
	s_add_u32 s30, s16, s33
	s_addc_u32 s31, s31, s35
	s_add_u32 s34, s4, s33
	s_addc_u32 s35, s5, s35
	s_add_i32 s16, s19, s27
	s_add_i32 m0, s16, 0x4000
	s_nop 0
	global_load_lds_dwordx4 v84, s[30:31]
	v_add_u32_e32 v0, s29, v91
	ds_read_b128 v[130:133], v0
	ds_read_b128 v[134:137], v0 offset:1024
	ds_read_b128 v[138:141], v0 offset:2048
	s_add_i32 m0, s16, 0x6000
	s_nop 0
	global_load_lds_dwordx4 v88, s[30:31]
	ds_read_b128 v[142:145], v0 offset:3072
	ds_read_b128 v[146:149], v0 offset:4096
	ds_read_b128 v[150:153], v0 offset:5120
	s_mov_b32 m0, s16
	s_nop 0
	global_load_lds_dwordx4 v82, s[34:35]
	ds_read_b128 v[154:157], v0 offset:6144
	ds_read_b128 v[158:161], v0 offset:7168
	s_waitcnt vmcnt(3)
	s_waitcnt lgkmcnt(0)
	s_barrier
	s_setprio 1
	s_waitcnt lgkmcnt(0)
	v_mfma_f32_16x16x32_f16 v[78:81], v[94:97], v[130:133], v[78:81]
	s_add_u32 s30, s30, 0x40000
	s_addc_u32 s31, s31, 0
	s_add_i32 m0, s16, 0x8000
	v_mfma_f32_16x16x32_f16 v[74:77], v[106:109], v[130:133], v[74:77]
	global_load_lds_dwordx4 v84, s[30:31]
	s_add_i32 m0, s16, 0xa000
	v_mfma_f32_16x16x32_f16 v[66:69], v[94:97], v[138:141], v[66:69]
	global_load_lds_dwordx4 v88, s[30:31]
	s_add_i32 m0, s16, 0x2000
	v_mfma_f32_16x16x32_f16 v[58:61], v[106:109], v[138:141], v[58:61]
	global_load_lds_dwordx4 v86, s[34:35]
	v_mfma_f32_16x16x32_f16 v[78:81], v[102:105], v[134:137], v[78:81]
	v_mfma_f32_16x16x32_f16 v[74:77], v[110:113], v[134:137], v[74:77]
	v_mfma_f32_16x16x32_f16 v[66:69], v[102:105], v[142:145], v[66:69]
	v_mfma_f32_16x16x32_f16 v[58:61], v[110:113], v[142:145], v[58:61]
	v_mfma_f32_16x16x32_f16 v[54:57], v[94:97], v[146:149], v[54:57]
	v_mfma_f32_16x16x32_f16 v[46:49], v[106:109], v[146:149], v[46:49]
	v_mfma_f32_16x16x32_f16 v[34:37], v[94:97], v[154:157], v[34:37]
	v_mfma_f32_16x16x32_f16 v[26:29], v[106:109], v[154:157], v[26:29]
	v_mfma_f32_16x16x32_f16 v[54:57], v[102:105], v[150:153], v[54:57]
	v_mfma_f32_16x16x32_f16 v[46:49], v[110:113], v[150:153], v[46:49]
	v_mfma_f32_16x16x32_f16 v[34:37], v[102:105], v[158:161], v[34:37]
	v_mfma_f32_16x16x32_f16 v[26:29], v[110:113], v[158:161], v[26:29]
	v_mfma_f32_16x16x32_f16 v[70:73], v[114:117], v[130:133], v[70:73]
	v_mfma_f32_16x16x32_f16 v[62:65], v[122:125], v[130:133], v[62:65]
	v_mfma_f32_16x16x32_f16 v[50:53], v[114:117], v[138:141], v[50:53]
	v_mfma_f32_16x16x32_f16 v[42:45], v[122:125], v[138:141], v[42:45]
	v_mfma_f32_16x16x32_f16 v[70:73], v[118:121], v[134:137], v[70:73]
	v_mfma_f32_16x16x32_f16 v[62:65], v[126:129], v[134:137], v[62:65]
	v_mfma_f32_16x16x32_f16 v[50:53], v[118:121], v[142:145], v[50:53]
	v_mfma_f32_16x16x32_f16 v[42:45], v[126:129], v[142:145], v[42:45]
	v_mfma_f32_16x16x32_f16 v[38:41], v[114:117], v[146:149], v[38:41]
	v_mfma_f32_16x16x32_f16 v[30:33], v[122:125], v[146:149], v[30:33]
	s_add_i32 s3, s3, 1
	s_bitcmp1_b32 s3, 4
	s_addc_u32 s28, s28, 0
	v_mfma_f32_16x16x32_f16 v[22:25], v[114:117], v[154:157], v[22:25]
	s_and_b32 s3, s3, 15
	v_mfma_f32_16x16x32_f16 v[2:5], v[122:125], v[154:157], v[2:5]
	v_mfma_f32_16x16x32_f16 v[38:41], v[118:121], v[150:153], v[38:41]
	v_mfma_f32_16x16x32_f16 v[30:33], v[126:129], v[150:153], v[30:33]
	s_add_i32 s26, s26, -1
	v_mfma_f32_16x16x32_f16 v[22:25], v[118:121], v[158:161], v[22:25]
	s_mov_b32 s16, s24
	s_mov_b32 s24, s27
	v_mfma_f32_16x16x32_f16 v[2:5], v[126:129], v[158:161], v[2:5]
	s_mov_b32 s27, s29
	s_cmp_lg_u32 s26, 0
	s_setprio 0
	s_barrier
	s_cbranch_scc1 .LBB1_3
	s_lshl_b32 s3, s14, 7
	s_add_i32 s17, s25, s3
	s_ashr_i32 s3, s17, 1
	s_lshr_b32 s14, s17, 5
	s_or_b32 s24, s15, s2
	s_and_b32 s14, s14, 62
	s_and_b32 s27, s3, 0xfffffc00
	v_or_b32_e32 v105, s24, v1
	v_lshlrev_b32_e32 v98, 4, v93
	v_or_b32_e32 v102, 16, v93
	v_or_b32_e32 v103, 32, v93
	v_or_b32_e32 v104, 48, v93
	v_mov_b32_e32 v93, 0
	s_and_b32 s16, s24, 0x340
	v_lshlrev_b32_e32 v95, 6, v105
	s_or_b32 s2, s27, s14
	v_lshlrev_b32_e32 v0, 9, v92
	v_and_b32_e32 v110, 0xc00, v95
	v_mov_b32_e32 v111, v93
	s_or_b32 s14, s2, s16
	v_and_b32_e32 v92, 0x200, v0
	v_lshl_add_u64 v[110:111], s[8:9], 0, v[110:111]
	s_or_b32 s30, s14, 0x80
	s_mov_b32 s3, 0
	v_mov_b32_e32 v99, v93
	v_lshl_add_u64 v[110:111], v[110:111], 0, v[92:93]
	s_mov_b32 s2, 0x3e38aa3b
	v_pk_add_f32 v[72:73], v[12:13], v[72:73]
	v_pk_add_f32 v[70:71], v[10:11], v[70:71]
	v_pk_add_f32 v[64:65], v[8:9], v[64:65]
	v_pk_add_f32 v[62:63], v[6:7], v[62:63]
	s_ashr_i32 s31, s30, 31
	v_lshl_add_u64 v[112:113], v[110:111], 0, v[98:99]
	v_pk_mul_f32 v[72:73], v[72:73], s[2:3] op_sel_hi:[1,0]
	v_pk_mul_f32 v[70:71], v[70:71], s[2:3] op_sel_hi:[1,0]
	v_pk_mul_f32 v[64:65], v[64:65], s[2:3] op_sel_hi:[1,0]
	v_pk_mul_f32 v[62:63], v[62:63], s[2:3] op_sel_hi:[1,0]
	s_lshl_b64 s[30:31], s[30:31], 12
	v_lshlrev_b32_e32 v96, 4, v102
	v_mov_b32_e32 v97, v93
	v_pk_add_f32 v[80:81], v[20:21], v[80:81]
	v_pk_add_f32 v[78:79], v[18:19], v[78:79]
	v_pk_add_f32 v[74:75], v[14:15], v[74:75]
	s_ashr_i32 s15, s14, 31
	v_cvt_pk_f16_f32 v70, v70, v71
	v_cvt_pk_f16_f32 v71, v72, v73
	v_cvt_pk_f16_f32 v72, v62, v63
	v_cvt_pk_f16_f32 v73, v64, v65
	v_lshl_add_u64 v[62:63], v[112:113], 0, s[30:31]
	v_pk_add_f32 v[58:59], v[14:15], v[58:59]
	v_pk_mul_f32 v[80:81], v[80:81], s[2:3] op_sel_hi:[1,0]
	v_pk_mul_f32 v[78:79], v[78:79], s[2:3] op_sel_hi:[1,0]
	v_pk_mul_f32 v[74:75], v[74:75], s[2:3] op_sel_hi:[1,0]
	s_lshl_b64 s[28:29], s[14:15], 12
	global_store_dwordx4 v[62:63], v[70:73], off
	v_pk_add_f32 v[62:63], v[20:21], v[68:69]
	v_pk_add_f32 v[64:65], v[18:19], v[66:67]
	v_lshl_add_u64 v[70:71], v[110:111], 0, v[96:97]
	v_pk_mul_f32 v[58:59], v[58:59], s[2:3] op_sel_hi:[1,0]
	v_pk_add_f32 v[52:53], v[12:13], v[52:53]
	v_pk_add_f32 v[50:51], v[10:11], v[50:51]
	v_pk_add_f32 v[44:45], v[8:9], v[44:45]
	v_pk_add_f32 v[42:43], v[6:7], v[42:43]
	v_lshlrev_b32_e32 v0, 4, v103
	v_cvt_pk_f16_f32 v78, v78, v79
	v_cvt_pk_f16_f32 v79, v80, v81
	v_cvt_pk_f16_f32 v80, v74, v75
	v_lshl_add_u64 v[74:75], v[112:113], 0, s[28:29]
	v_pk_mul_f32 v[66:67], v[62:63], s[2:3] op_sel_hi:[1,0]
	v_pk_mul_f32 v[62:63], v[64:65], s[2:3] op_sel_hi:[1,0]
	v_cvt_pk_f16_f32 v64, v58, v59
	v_lshl_add_u64 v[58:59], v[70:71], 0, s[28:29]
	v_pk_mul_f32 v[52:53], v[52:53], s[2:3] op_sel_hi:[1,0]
	v_pk_mul_f32 v[50:51], v[50:51], s[2:3] op_sel_hi:[1,0]
	v_pk_mul_f32 v[44:45], v[44:45], s[2:3] op_sel_hi:[1,0]
	v_pk_mul_f32 v[42:43], v[42:43], s[2:3] op_sel_hi:[1,0]
	s_or_b32 s28, s14, 1
	s_or_b32 s14, s14, 0x81
	v_and_b32_e32 v106, 0xf0, v0
	v_mov_b32_e32 v107, v93
	v_cvt_pk_f16_f32 v50, v50, v51
	v_cvt_pk_f16_f32 v51, v52, v53
	v_cvt_pk_f16_f32 v52, v42, v43
	v_cvt_pk_f16_f32 v53, v44, v45
	v_lshl_add_u64 v[42:43], v[70:71], 0, s[30:31]
	v_pk_add_f32 v[40:41], v[12:13], v[40:41]
	v_pk_add_f32 v[38:39], v[10:11], v[38:39]
	v_pk_add_f32 v[32:33], v[8:9], v[32:33]
	v_pk_add_f32 v[30:31], v[6:7], v[30:31]
	s_ashr_i32 s15, s14, 31
	v_lshlrev_b32_e32 v94, 4, v104
	global_store_dwordx4 v[42:43], v[50:53], off
	v_pk_mul_f32 v[40:41], v[40:41], s[2:3] op_sel_hi:[1,0]
	v_pk_mul_f32 v[38:39], v[38:39], s[2:3] op_sel_hi:[1,0]
	v_lshl_add_u64 v[50:51], v[110:111], 0, v[106:107]
	v_pk_mul_f32 v[32:33], v[32:33], s[2:3] op_sel_hi:[1,0]
	v_pk_mul_f32 v[30:31], v[30:31], s[2:3] op_sel_hi:[1,0]
	s_lshl_b64 s[14:15], s[14:15], 12
	v_and_b32_e32 v108, 0x1f0, v94
	v_mov_b32_e32 v109, v93
	v_pk_add_f32 v[42:43], v[20:21], v[56:57]
	v_pk_add_f32 v[44:45], v[18:19], v[54:55]
	v_pk_add_f32 v[46:47], v[14:15], v[46:47]
	s_ashr_i32 s29, s28, 31
	v_cvt_pk_f16_f32 v38, v38, v39
	v_cvt_pk_f16_f32 v39, v40, v41
	v_cvt_pk_f16_f32 v40, v30, v31
	v_cvt_pk_f16_f32 v41, v32, v33
	v_lshl_add_u64 v[30:31], v[50:51], 0, s[14:15]
	v_pk_add_f32 v[20:21], v[20:21], v[36:37]
	v_pk_add_f32 v[18:19], v[18:19], v[34:35]
	v_pk_add_f32 v[14:15], v[14:15], v[26:27]
	v_pk_add_f32 v[76:77], v[16:17], v[76:77]
	v_pk_add_f32 v[60:61], v[16:17], v[60:61]
	v_pk_mul_f32 v[52:53], v[42:43], s[2:3] op_sel_hi:[1,0]
	v_pk_mul_f32 v[42:43], v[44:45], s[2:3] op_sel_hi:[1,0]
	v_pk_add_f32 v[44:45], v[16:17], v[48:49]
	s_lshl_b64 s[28:29], s[28:29], 12
	global_store_dwordx4 v[30:31], v[38:41], off
	v_lshl_add_u64 v[30:31], v[110:111], 0, v[108:109]
	v_pk_mul_f32 v[20:21], v[20:21], s[2:3] op_sel_hi:[1,0]
	v_pk_mul_f32 v[18:19], v[18:19], s[2:3] op_sel_hi:[1,0]
	v_pk_add_f32 v[16:17], v[16:17], v[28:29]
	v_pk_mul_f32 v[14:15], v[14:15], s[2:3] op_sel_hi:[1,0]
	v_pk_add_f32 v[12:13], v[12:13], v[24:25]
	v_pk_add_f32 v[10:11], v[10:11], v[22:23]
	v_pk_add_f32 v[4:5], v[8:9], v[4:5]
	v_pk_add_f32 v[2:3], v[6:7], v[2:3]
	v_pk_mul_f32 v[76:77], v[76:77], s[2:3] op_sel_hi:[1,0]
	v_pk_mul_f32 v[60:61], v[60:61], s[2:3] op_sel_hi:[1,0]
	v_pk_mul_f32 v[48:49], v[44:45], s[2:3] op_sel_hi:[1,0]
	v_pk_mul_f32 v[44:45], v[46:47], s[2:3] op_sel_hi:[1,0]
	v_lshl_add_u64 v[46:47], v[50:51], 0, s[28:29]
	v_cvt_pk_f16_f32 v18, v18, v19
	v_cvt_pk_f16_f32 v19, v20, v21
	v_pk_mul_f32 v[16:17], v[16:17], s[2:3] op_sel_hi:[1,0]
	v_cvt_pk_f16_f32 v20, v14, v15
	v_lshl_add_u64 v[14:15], v[30:31], 0, s[28:29]
	v_pk_mul_f32 v[12:13], v[12:13], s[2:3] op_sel_hi:[1,0]
	v_pk_mul_f32 v[10:11], v[10:11], s[2:3] op_sel_hi:[1,0]
	v_pk_mul_f32 v[4:5], v[4:5], s[2:3] op_sel_hi:[1,0]
	v_pk_mul_f32 v[2:3], v[2:3], s[2:3] op_sel_hi:[1,0]
	s_add_u32 s28, s20, s22
	v_cvt_pk_f16_f32 v81, v76, v77
	v_cvt_pk_f16_f32 v62, v62, v63
	v_cvt_pk_f16_f32 v63, v66, v67
	v_cvt_pk_f16_f32 v65, v60, v61
	v_cvt_pk_f16_f32 v42, v42, v43
	v_cvt_pk_f16_f32 v43, v52, v53
	v_cvt_pk_f16_f32 v44, v44, v45
	v_cvt_pk_f16_f32 v45, v48, v49
	v_cvt_pk_f16_f32 v21, v16, v17
	v_cvt_pk_f16_f32 v10, v10, v11
	v_cvt_pk_f16_f32 v11, v12, v13
	v_cvt_pk_f16_f32 v12, v2, v3
	v_cvt_pk_f16_f32 v13, v4, v5
	v_lshl_add_u64 v[2:3], v[30:31], 0, s[14:15]
	s_addc_u32 s29, s21, 0
	v_lshlrev_b32_e32 v92, 2, v1
	global_store_dwordx4 v[74:75], v[78:81], off
	global_store_dwordx4 v[58:59], v[62:65], off
	global_store_dwordx4 v[46:47], v[42:45], off
	global_store_dwordx4 v[14:15], v[18:21], off
	global_store_dwordx4 v[2:3], v[10:13], off
	v_lshl_add_u64 v[2:3], s[28:29], 0, v[92:93]
	s_mov_b64 s[28:29], 0x1000
	v_lshl_add_u64 v[10:11], v[2:3], 0, s[28:29]
	global_load_dwordx4 v[22:25], v[10:11], off
	global_load_dwordx4 v[14:17], v[10:11], off offset:16
	global_load_dwordx4 v[6:9], v[10:11], off offset:512
	global_load_dwordx4 v[2:5], v[10:11], off offset:528
	s_mov_b32 s25, 1
	s_mov_b32 s26, 16
	s_mov_b32 s14, 2
	s_mov_b32 s15, 0x18000
	s_mov_b32 s2, 0xc000
	s_mov_b32 s27, 0
	v_mov_b32_e32 v10, v93
	v_mov_b32_e32 v11, v93
	v_mov_b32_e32 v12, v93
	v_mov_b32_e32 v13, v93
	v_mov_b32_e32 v18, v93
	v_mov_b32_e32 v19, v93
	v_mov_b32_e32 v20, v93
	v_mov_b32_e32 v21, v93
	v_mov_b32_e32 v26, v93
	v_mov_b32_e32 v27, v93
	v_mov_b32_e32 v28, v93
	v_mov_b32_e32 v29, v93
	v_mov_b32_e32 v34, v93
	v_mov_b32_e32 v35, v93
	v_mov_b32_e32 v36, v93
	v_mov_b32_e32 v37, v93
	v_mov_b32_e32 v42, v93
	v_mov_b32_e32 v43, v93
	v_mov_b32_e32 v44, v93
	v_mov_b32_e32 v45, v93
	v_mov_b32_e32 v50, v93
	v_mov_b32_e32 v51, v93
	v_mov_b32_e32 v52, v93
	v_mov_b32_e32 v53, v93
	v_mov_b32_e32 v62, v93
	v_mov_b32_e32 v63, v93
	v_mov_b32_e32 v64, v93
	v_mov_b32_e32 v65, v93
	v_mov_b32_e32 v70, v93
	v_mov_b32_e32 v71, v93
	v_mov_b32_e32 v72, v93
	v_mov_b32_e32 v73, v93
	v_mov_b32_e32 v30, v93
	v_mov_b32_e32 v31, v93
	v_mov_b32_e32 v32, v93
	v_mov_b32_e32 v33, v93
	v_mov_b32_e32 v38, v93
	v_mov_b32_e32 v39, v93
	v_mov_b32_e32 v40, v93
	v_mov_b32_e32 v41, v93
	v_mov_b32_e32 v46, v93
	v_mov_b32_e32 v47, v93
	v_mov_b32_e32 v48, v93
	v_mov_b32_e32 v49, v93
	v_mov_b32_e32 v54, v93
	v_mov_b32_e32 v55, v93
	v_mov_b32_e32 v56, v93
	v_mov_b32_e32 v57, v93
	v_mov_b32_e32 v58, v93
	v_mov_b32_e32 v59, v93
	v_mov_b32_e32 v60, v93
	v_mov_b32_e32 v61, v93
	v_mov_b32_e32 v66, v93
	v_mov_b32_e32 v67, v93
	v_mov_b32_e32 v68, v93
	v_mov_b32_e32 v69, v93
	v_mov_b32_e32 v74, v93
	v_mov_b32_e32 v75, v93
	v_mov_b32_e32 v76, v93
	v_mov_b32_e32 v77, v93
	v_mov_b32_e32 v78, v93
	v_mov_b32_e32 v79, v93
	v_mov_b32_e32 v80, v93
	v_mov_b32_e32 v81, v93
.LBB1_5:
	s_mov_b32 s28, s2
	v_add_u32_e32 v1, s28, v101
	ds_read_b128 v[106:109], v1 offset:16384
	ds_read_b128 v[110:113], v1 offset:17408
	ds_read_b128 v[114:117], v1 offset:18432
	ds_read_b128 v[118:121], v1 offset:19456
	ds_read_b128 v[122:125], v1 offset:32768
	ds_read_b128 v[126:129], v1 offset:33792
	ds_read_b128 v[130:133], v1 offset:34816
	ds_read_b128 v[134:137], v1 offset:35840
	s_lshl_b32 s2, s25, 2
	s_or_b32 s2, s2, s23
	s_lshl_b64 s[30:31], s[2:3], 19
	s_add_u32 s2, s6, s30
	s_addc_u32 s29, s7, s31
	s_lshl_b32 s33, s14, 7
	s_ashr_i32 s35, s33, 31
	s_add_u32 s30, s2, s33
	s_addc_u32 s31, s29, s35
	s_add_u32 s34, s4, s33
	s_addc_u32 s35, s5, s35
	s_add_i32 s2, s19, s27
	s_add_i32 m0, s2, 0x4000
	s_nop 0
	global_load_lds_dwordx4 v84, s[30:31]
	v_add_u32_e32 v1, s28, v91
	ds_read_b128 v[138:141], v1
	ds_read_b128 v[142:145], v1 offset:1024
	ds_read_b128 v[146:149], v1 offset:2048
	s_add_i32 m0, s2, 0x6000
	s_nop 0
	global_load_lds_dwordx4 v88, s[30:31]
	ds_read_b128 v[150:153], v1 offset:3072
	ds_read_b128 v[154:157], v1 offset:4096
	ds_read_b128 v[158:161], v1 offset:5120
	s_mov_b32 m0, s2
	s_nop 0
	global_load_lds_dwordx4 v82, s[34:35]
	ds_read_b128 v[162:165], v1 offset:6144
	ds_read_b128 v[166:169], v1 offset:7168
	s_waitcnt vmcnt(3)
	s_waitcnt lgkmcnt(0)
	s_barrier
	s_setprio 1
	s_waitcnt lgkmcnt(0)
	v_mfma_f32_16x16x32_f16 v[78:81], v[106:109], v[138:141], v[78:81]
	s_add_u32 s30, s30, 0x40000
	s_addc_u32 s31, s31, 0
	s_add_i32 m0, s2, 0x8000
	v_mfma_f32_16x16x32_f16 v[74:77], v[114:117], v[138:141], v[74:77]
	global_load_lds_dwordx4 v84, s[30:31]
	s_add_i32 m0, s2, 0xa000
	v_mfma_f32_16x16x32_f16 v[66:69], v[106:109], v[146:149], v[66:69]
	global_load_lds_dwordx4 v88, s[30:31]
	s_add_i32 m0, s2, 0x2000
	v_mfma_f32_16x16x32_f16 v[58:61], v[114:117], v[146:149], v[58:61]
	global_load_lds_dwordx4 v86, s[34:35]
	v_mfma_f32_16x16x32_f16 v[78:81], v[110:113], v[142:145], v[78:81]
	v_mfma_f32_16x16x32_f16 v[74:77], v[118:121], v[142:145], v[74:77]
	v_mfma_f32_16x16x32_f16 v[66:69], v[110:113], v[150:153], v[66:69]
	v_mfma_f32_16x16x32_f16 v[58:61], v[118:121], v[150:153], v[58:61]
	v_mfma_f32_16x16x32_f16 v[54:57], v[106:109], v[154:157], v[54:57]
	v_mfma_f32_16x16x32_f16 v[46:49], v[114:117], v[154:157], v[46:49]
	v_mfma_f32_16x16x32_f16 v[38:41], v[106:109], v[162:165], v[38:41]
	v_mfma_f32_16x16x32_f16 v[30:33], v[114:117], v[162:165], v[30:33]
	v_mfma_f32_16x16x32_f16 v[54:57], v[110:113], v[158:161], v[54:57]
	v_mfma_f32_16x16x32_f16 v[46:49], v[118:121], v[158:161], v[46:49]
	v_mfma_f32_16x16x32_f16 v[38:41], v[110:113], v[166:169], v[38:41]
	v_mfma_f32_16x16x32_f16 v[30:33], v[118:121], v[166:169], v[30:33]
	v_mfma_f32_16x16x32_f16 v[70:73], v[122:125], v[138:141], v[70:73]
	v_mfma_f32_16x16x32_f16 v[62:65], v[130:133], v[138:141], v[62:65]
	v_mfma_f32_16x16x32_f16 v[50:53], v[122:125], v[146:149], v[50:53]
	v_mfma_f32_16x16x32_f16 v[42:45], v[130:133], v[146:149], v[42:45]
	v_mfma_f32_16x16x32_f16 v[70:73], v[126:129], v[142:145], v[70:73]
	v_mfma_f32_16x16x32_f16 v[62:65], v[134:137], v[142:145], v[62:65]
	v_mfma_f32_16x16x32_f16 v[50:53], v[126:129], v[150:153], v[50:53]
	v_mfma_f32_16x16x32_f16 v[42:45], v[134:137], v[150:153], v[42:45]
	v_mfma_f32_16x16x32_f16 v[34:37], v[122:125], v[154:157], v[34:37]
	v_mfma_f32_16x16x32_f16 v[26:29], v[130:133], v[154:157], v[26:29]
	s_add_i32 s14, s14, 1
	s_bitcmp1_b32 s14, 4
	s_addc_u32 s25, s25, 0
	v_mfma_f32_16x16x32_f16 v[18:21], v[122:125], v[162:165], v[18:21]
	s_and_b32 s14, s14, 15
	v_mfma_f32_16x16x32_f16 v[10:13], v[130:133], v[162:165], v[10:13]
	v_mfma_f32_16x16x32_f16 v[34:37], v[126:129], v[158:161], v[34:37]
	v_mfma_f32_16x16x32_f16 v[26:29], v[134:137], v[158:161], v[26:29]
	s_add_i32 s26, s26, -1
	v_mfma_f32_16x16x32_f16 v[18:21], v[126:129], v[166:169], v[18:21]
	s_mov_b32 s2, s15
	s_mov_b32 s15, s27
	v_mfma_f32_16x16x32_f16 v[10:13], v[134:137], v[166:169], v[10:13]
	s_mov_b32 s27, s28
	s_cmp_lg_u32 s26, 0
	s_setprio 0
	s_barrier
	s_cbranch_scc1 .LBB1_5
	s_ashr_i32 s2, s17, 7
	s_and_b32 s3, s2, -16
	s_or_b32 s2, s3, 2
	s_sub_u32 s14, s10, s8
	s_subb_u32 s11, s11, s9
	s_bfe_u32 s6, s17, 0x50006
	s_add_u32 s14, s8, s14
	s_addc_u32 s15, s9, s11
	s_lshr_b32 s11, s24, 6
	s_or_b32 s17, s11, s3
	s_lshl_b32 s17, s17, 8
	s_lshl_b32 s23, s6, 3
	v_bfe_u32 v93, v105, 3, 3
	v_pk_add_f32 v[80:81], v[24:25], v[80:81]
	v_pk_add_f32 v[78:79], v[22:23], v[78:79]
	v_pk_add_f32 v[74:75], v[14:15], v[74:75]
	s_or_b32 s17, s17, s23
	s_or_b32 s11, s2, s11
	v_cvt_pk_f16_f32 v78, v78, v79
	v_cvt_pk_f16_f32 v79, v80, v81
	v_cvt_pk_f16_f32 v80, v74, v75
	v_or_b32_e32 v74, s17, v93
	s_lshl_b32 s11, s11, 8
	v_ashrrev_i32_e32 v75, 31, v74
	v_pk_add_f32 v[72:73], v[8:9], v[72:73]
	v_pk_add_f32 v[70:71], v[6:7], v[70:71]
	v_pk_add_f32 v[62:63], v[2:3], v[62:63]
	s_or_b32 s11, s11, s23
	v_lshlrev_b64 v[74:75], 10, v[74:75]
	v_cvt_pk_f16_f32 v70, v70, v71
	v_cvt_pk_f16_f32 v71, v72, v73
	v_cvt_pk_f16_f32 v72, v62, v63
	v_or_b32_e32 v62, s11, v93
	v_pk_add_f32 v[76:77], v[16:17], v[76:77]
	v_lshl_add_u64 v[74:75], s[14:15], 0, v[74:75]
	v_ashrrev_i32_e32 v63, 31, v62
	v_cvt_pk_f16_f32 v81, v76, v77
	v_lshl_add_u64 v[76:77], v[74:75], 0, v[98:99]
	v_lshlrev_b64 v[62:63], 10, v[62:63]
	global_store_dwordx4 v[76:77], v[78:81], off
	v_pk_add_f32 v[64:65], v[4:5], v[64:65]
	v_lshl_add_u64 v[76:77], s[14:15], 0, v[62:63]
	v_cvt_pk_f16_f32 v73, v64, v65
	v_lshl_add_u64 v[62:63], v[76:77], 0, v[98:99]
	global_store_dwordx4 v[62:63], v[70:73], off
	v_pk_add_f32 v[64:65], v[24:25], v[68:69]
	v_pk_add_f32 v[62:63], v[22:23], v[66:67]
	v_pk_add_f32 v[60:61], v[16:17], v[60:61]
	v_pk_add_f32 v[58:59], v[14:15], v[58:59]
	v_pk_add_f32 v[52:53], v[8:9], v[52:53]
	v_pk_add_f32 v[50:51], v[6:7], v[50:51]
	v_pk_add_f32 v[44:45], v[4:5], v[44:45]
	v_pk_add_f32 v[42:43], v[2:3], v[42:43]
	v_cvt_pk_f16_f32 v62, v62, v63
	v_cvt_pk_f16_f32 v63, v64, v65
	v_cvt_pk_f16_f32 v64, v58, v59
	v_cvt_pk_f16_f32 v65, v60, v61
	v_lshl_add_u64 v[58:59], v[74:75], 0, v[96:97]
	v_cvt_pk_f16_f32 v50, v50, v51
	v_cvt_pk_f16_f32 v51, v52, v53
	v_cvt_pk_f16_f32 v52, v42, v43
	v_cvt_pk_f16_f32 v53, v44, v45
	v_lshl_add_u64 v[42:43], v[76:77], 0, v[96:97]
	v_mov_b32_e32 v1, 0
	global_store_dwordx4 v[58:59], v[62:65], off
	global_store_dwordx4 v[42:43], v[50:53], off
	v_pk_add_f32 v[44:45], v[24:25], v[56:57]
	v_pk_add_f32 v[42:43], v[22:23], v[54:55]
	v_mov_b32_e32 v95, v1
	v_cvt_pk_f16_f32 v42, v42, v43
	v_cvt_pk_f16_f32 v43, v44, v45
	v_pk_add_f32 v[48:49], v[16:17], v[48:49]
	v_pk_add_f32 v[44:45], v[14:15], v[46:47]
	v_pk_add_f32 v[36:37], v[8:9], v[36:37]
	v_pk_add_f32 v[34:35], v[6:7], v[34:35]
	v_pk_add_f32 v[28:29], v[4:5], v[28:29]
	v_pk_add_f32 v[26:27], v[2:3], v[26:27]
	v_pk_add_f32 v[24:25], v[24:25], v[40:41]
	v_pk_add_f32 v[22:23], v[22:23], v[38:39]
	v_pk_add_f32 v[16:17], v[16:17], v[32:33]
	v_pk_add_f32 v[14:15], v[14:15], v[30:31]
	v_pk_add_f32 v[8:9], v[8:9], v[20:21]
	v_pk_add_f32 v[6:7], v[6:7], v[18:19]
	v_pk_add_f32 v[4:5], v[4:5], v[12:13]
	v_pk_add_f32 v[2:3], v[2:3], v[10:11]
	s_add_u32 s14, s20, s22
	v_cvt_pk_f16_f32 v44, v44, v45
	v_cvt_pk_f16_f32 v45, v48, v49
	v_lshl_add_u64 v[46:47], v[74:75], 0, v[0:1]
	v_cvt_pk_f16_f32 v34, v34, v35
	v_cvt_pk_f16_f32 v35, v36, v37
	v_cvt_pk_f16_f32 v36, v26, v27
	v_cvt_pk_f16_f32 v37, v28, v29
	v_lshl_add_u64 v[26:27], v[76:77], 0, v[0:1]
	v_cvt_pk_f16_f32 v22, v22, v23
	v_cvt_pk_f16_f32 v23, v24, v25
	v_cvt_pk_f16_f32 v24, v14, v15
	v_cvt_pk_f16_f32 v25, v16, v17
	v_lshl_add_u64 v[14:15], v[74:75], 0, v[94:95]
	v_cvt_pk_f16_f32 v6, v6, v7
	v_cvt_pk_f16_f32 v7, v8, v9
	v_cvt_pk_f16_f32 v8, v2, v3
	v_cvt_pk_f16_f32 v9, v4, v5
	v_lshl_add_u64 v[2:3], v[76:77], 0, v[94:95]
	s_addc_u32 s15, s21, 0
	v_mov_b32_e32 v93, v1
	global_store_dwordx4 v[46:47], v[42:45], off
	global_store_dwordx4 v[26:27], v[34:37], off
	global_store_dwordx4 v[14:15], v[22:25], off
	global_store_dwordx4 v[2:3], v[6:9], off
	v_lshl_add_u64 v[2:3], s[14:15], 0, v[92:93]
	s_mov_b64 s[14:15], 0x2000
	v_lshl_add_u64 v[2:3], v[2:3], 0, s[14:15]
	global_load_dwordx4 v[20:23], v[2:3], off
	global_load_dwordx4 v[12:15], v[2:3], off offset:16
	global_load_dwordx4 v[8:11], v[2:3], off offset:512
	global_load_dwordx4 v[4:7], v[2:3], off offset:528
	s_add_u32 s11, s12, 0x400000
	s_mov_b32 s7, 2
	v_and_b32_e32 v106, 56, v105
	s_mov_b32 s10, 0
	s_addc_u32 s12, s13, 0
	s_mov_b32 s14, 0xc000
	s_mov_b32 s17, 0x18000
	s_mov_b32 s13, 16
	v_mov_b32_e32 v0, v1
	v_mov_b32_e32 v2, v1
	v_mov_b32_e32 v3, v1
	v_mov_b32_e32 v16, v1
	v_mov_b32_e32 v17, v1
	v_mov_b32_e32 v18, v1
	v_mov_b32_e32 v19, v1
	v_mov_b32_e32 v24, v1
	v_mov_b32_e32 v25, v1
	v_mov_b32_e32 v26, v1
	v_mov_b32_e32 v27, v1
	v_mov_b32_e32 v32, v1
	v_mov_b32_e32 v33, v1
	v_mov_b32_e32 v34, v1
	v_mov_b32_e32 v35, v1
	v_mov_b32_e32 v40, v1
	v_mov_b32_e32 v41, v1
	v_mov_b32_e32 v42, v1
	v_mov_b32_e32 v43, v1
	v_mov_b32_e32 v48, v1
	v_mov_b32_e32 v49, v1
	v_mov_b32_e32 v50, v1
	v_mov_b32_e32 v51, v1
	v_mov_b32_e32 v60, v1
	v_mov_b32_e32 v61, v1
	v_mov_b32_e32 v62, v1
	v_mov_b32_e32 v63, v1
	v_mov_b32_e32 v68, v1
	v_mov_b32_e32 v69, v1
	v_mov_b32_e32 v70, v1
	v_mov_b32_e32 v71, v1
	v_mov_b32_e32 v28, v1
	v_mov_b32_e32 v29, v1
	v_mov_b32_e32 v30, v1
	v_mov_b32_e32 v31, v1
	v_mov_b32_e32 v36, v1
	v_mov_b32_e32 v37, v1
	v_mov_b32_e32 v38, v1
	v_mov_b32_e32 v39, v1
	v_mov_b32_e32 v44, v1
	v_mov_b32_e32 v45, v1
	v_mov_b32_e32 v46, v1
	v_mov_b32_e32 v47, v1
	v_mov_b32_e32 v52, v1
	v_mov_b32_e32 v53, v1
	v_mov_b32_e32 v54, v1
	v_mov_b32_e32 v55, v1
	v_mov_b32_e32 v56, v1
	v_mov_b32_e32 v57, v1
	v_mov_b32_e32 v58, v1
	v_mov_b32_e32 v59, v1
	v_mov_b32_e32 v64, v1
	v_mov_b32_e32 v65, v1
	v_mov_b32_e32 v66, v1
	v_mov_b32_e32 v67, v1
	v_mov_b32_e32 v72, v1
	v_mov_b32_e32 v73, v1
	v_mov_b32_e32 v74, v1
	v_mov_b32_e32 v75, v1
	v_mov_b32_e32 v76, v1
	v_mov_b32_e32 v77, v1
	v_mov_b32_e32 v78, v1
	v_mov_b32_e32 v79, v1
.LBB1_7:
	s_mov_b32 s15, s17
	v_add_u32_e32 v80, s15, v101
	ds_read_b128 v[92:95], v80 offset:16384
	ds_read_b128 v[96:99], v80 offset:17408
	ds_read_b128 v[108:111], v80 offset:18432
	ds_read_b128 v[112:115], v80 offset:19456
	ds_read_b128 v[116:119], v80 offset:32768
	ds_read_b128 v[120:123], v80 offset:33792
	ds_read_b128 v[124:127], v80 offset:34816
	ds_read_b128 v[128:131], v80 offset:35840
	s_lshl_b32 s17, s7, 7
	s_ashr_i32 s23, s17, 31
	s_add_u32 s20, s11, s17
	s_addc_u32 s21, s12, s23
	s_add_u32 s22, s4, s17
	s_addc_u32 s23, s5, s23
	s_add_i32 s17, s19, s14
	s_add_i32 m0, s17, 0x4000
	s_nop 0
	global_load_lds_dwordx4 v84, s[20:21]
	v_add_u32_e32 v80, s15, v91
	ds_read_b128 v[132:135], v80
	ds_read_b128 v[136:139], v80 offset:1024
	ds_read_b128 v[140:143], v80 offset:2048
	s_add_i32 m0, s17, 0x6000
	s_nop 0
	global_load_lds_dwordx4 v88, s[20:21]
	ds_read_b128 v[144:147], v80 offset:3072
	ds_read_b128 v[148:151], v80 offset:4096
	ds_read_b128 v[152:155], v80 offset:5120
	s_mov_b32 m0, s17
	s_nop 0
	global_load_lds_dwordx4 v82, s[22:23]
	ds_read_b128 v[156:159], v80 offset:6144
	ds_read_b128 v[160:163], v80 offset:7168
	s_waitcnt vmcnt(3)
	s_waitcnt lgkmcnt(0)
	s_barrier
	s_setprio 1
	s_waitcnt lgkmcnt(0)
	v_mfma_f32_16x16x32_f16 v[76:79], v[92:95], v[132:135], v[76:79]
	s_add_u32 s20, s20, 0x40000
	s_addc_u32 s21, s21, 0
	s_add_i32 m0, s17, 0x8000
	v_mfma_f32_16x16x32_f16 v[72:75], v[108:111], v[132:135], v[72:75]
	global_load_lds_dwordx4 v84, s[20:21]
	s_add_i32 m0, s17, 0xa000
	v_mfma_f32_16x16x32_f16 v[64:67], v[92:95], v[140:143], v[64:67]
	global_load_lds_dwordx4 v88, s[20:21]
	s_add_i32 m0, s17, 0x2000
	v_mfma_f32_16x16x32_f16 v[56:59], v[108:111], v[140:143], v[56:59]
	global_load_lds_dwordx4 v86, s[22:23]
	v_mfma_f32_16x16x32_f16 v[76:79], v[96:99], v[136:139], v[76:79]
	v_mfma_f32_16x16x32_f16 v[72:75], v[112:115], v[136:139], v[72:75]
	v_mfma_f32_16x16x32_f16 v[64:67], v[96:99], v[144:147], v[64:67]
	v_mfma_f32_16x16x32_f16 v[56:59], v[112:115], v[144:147], v[56:59]
	v_mfma_f32_16x16x32_f16 v[52:55], v[92:95], v[148:151], v[52:55]
	v_mfma_f32_16x16x32_f16 v[44:47], v[108:111], v[148:151], v[44:47]
	v_mfma_f32_16x16x32_f16 v[36:39], v[92:95], v[156:159], v[36:39]
	v_mfma_f32_16x16x32_f16 v[28:31], v[108:111], v[156:159], v[28:31]
	v_mfma_f32_16x16x32_f16 v[52:55], v[96:99], v[152:155], v[52:55]
	v_mfma_f32_16x16x32_f16 v[44:47], v[112:115], v[152:155], v[44:47]
	v_mfma_f32_16x16x32_f16 v[36:39], v[96:99], v[160:163], v[36:39]
	v_mfma_f32_16x16x32_f16 v[28:31], v[112:115], v[160:163], v[28:31]
	v_mfma_f32_16x16x32_f16 v[68:71], v[116:119], v[132:135], v[68:71]
	v_mfma_f32_16x16x32_f16 v[60:63], v[124:127], v[132:135], v[60:63]
	v_mfma_f32_16x16x32_f16 v[48:51], v[116:119], v[140:143], v[48:51]
	v_mfma_f32_16x16x32_f16 v[40:43], v[124:127], v[140:143], v[40:43]
	v_mfma_f32_16x16x32_f16 v[68:71], v[120:123], v[136:139], v[68:71]
	v_mfma_f32_16x16x32_f16 v[60:63], v[128:131], v[136:139], v[60:63]
	v_mfma_f32_16x16x32_f16 v[48:51], v[120:123], v[144:147], v[48:51]
	v_mfma_f32_16x16x32_f16 v[40:43], v[128:131], v[144:147], v[40:43]
	v_mfma_f32_16x16x32_f16 v[32:35], v[116:119], v[148:151], v[32:35]
	v_mfma_f32_16x16x32_f16 v[24:27], v[124:127], v[148:151], v[24:27]
	s_add_i32 s7, s7, 1
	s_cmp_lg_u32 s7, 16
	v_mfma_f32_16x16x32_f16 v[16:19], v[116:119], v[156:159], v[16:19]
	s_cselect_b32 s7, s7, 0
	v_mfma_f32_16x16x32_f16 v[0:3], v[124:127], v[156:159], v[0:3]
	s_add_i32 s13, s13, -1
	v_mfma_f32_16x16x32_f16 v[32:35], v[120:123], v[152:155], v[32:35]
	s_mov_b32 s17, s10
	v_mfma_f32_16x16x32_f16 v[24:27], v[128:131], v[152:155], v[24:27]
	s_mov_b32 s10, s14
	v_mfma_f32_16x16x32_f16 v[16:19], v[120:123], v[160:163], v[16:19]
	s_mov_b32 s14, s15
	v_mfma_f32_16x16x32_f16 v[0:3], v[128:131], v[160:163], v[0:3]
	s_cmp_lg_u32 s13, 0
	s_setprio 0
	s_barrier
	s_cbranch_scc1 .LBB1_7
	s_sub_u32 s0, s0, s8
	s_subb_u32 s1, s1, s9
	s_add_u32 s0, s8, s0
	s_addc_u32 s1, s9, s1
	s_lshl_b32 s3, s3, 6
	s_or_b32 s3, s3, s16
	s_lshl_b32 s4, s6, 1
	v_lshrrev_b32_e32 v86, 5, v106
	v_pk_add_f32 v[78:79], v[22:23], v[78:79]
	v_pk_add_f32 v[76:77], v[20:21], v[76:77]
	v_pk_add_f32 v[72:73], v[12:13], v[72:73]
	s_or_b32 s3, s3, s4
	s_lshl_b32 s2, s2, 6
	v_cvt_pk_f16_f32 v76, v76, v77
	v_cvt_pk_f16_f32 v77, v78, v79
	v_cvt_pk_f16_f32 v78, v72, v73
	v_or_b32_e32 v72, s3, v86
	s_or_b32 s2, s2, s16
	v_ashrrev_i32_e32 v73, 31, v72
	v_pk_add_f32 v[70:71], v[10:11], v[70:71]
	v_pk_add_f32 v[68:69], v[8:9], v[68:69]
	v_pk_add_f32 v[60:61], v[4:5], v[60:61]
	s_or_b32 s2, s2, s4
	v_lshlrev_b64 v[72:73], 12, v[72:73]
	v_cvt_pk_f16_f32 v68, v68, v69
	v_cvt_pk_f16_f32 v69, v70, v71
	v_cvt_pk_f16_f32 v70, v60, v61
	v_or_b32_e32 v60, s2, v86
	v_mov_b32_e32 v91, 0
	v_pk_add_f32 v[74:75], v[14:15], v[74:75]
	v_lshl_add_u64 v[72:73], s[0:1], 0, v[72:73]
	v_ashrrev_i32_e32 v61, 31, v60
	v_cvt_pk_f16_f32 v79, v74, v75
	v_lshl_add_u64 v[74:75], v[72:73], 0, v[90:91]
	v_lshlrev_b64 v[60:61], 12, v[60:61]
	v_lshl_or_b32 v84, v102, 6, v100
	v_mov_b32_e32 v85, v91
	global_store_dwordx4 v[74:75], v[76:79], off sc1
	v_lshl_add_u64 v[74:75], s[0:1], 0, v[60:61]
	v_pk_add_f32 v[50:51], v[10:11], v[50:51]
	v_pk_add_f32 v[48:49], v[8:9], v[48:49]
	v_pk_add_f32 v[42:43], v[6:7], v[42:43]
	v_pk_add_f32 v[40:41], v[4:5], v[40:41]
	v_pk_add_f32 v[62:63], v[6:7], v[62:63]
	v_cvt_pk_f16_f32 v48, v48, v49
	v_cvt_pk_f16_f32 v49, v50, v51
	v_cvt_pk_f16_f32 v50, v40, v41
	v_cvt_pk_f16_f32 v51, v42, v43
	v_lshl_add_u64 v[40:41], v[74:75], 0, v[84:85]
	v_cvt_pk_f16_f32 v71, v62, v63
	v_lshl_add_u64 v[60:61], v[74:75], 0, v[90:91]
	global_store_dwordx4 v[40:41], v[48:51], off sc1
	v_pk_add_f32 v[42:43], v[22:23], v[54:55]
	v_pk_add_f32 v[40:41], v[20:21], v[52:53]
	v_lshl_or_b32 v80, v103, 6, v100
	v_lshl_or_b32 v82, v104, 6, v100
	v_mov_b32_e32 v81, v91
	v_mov_b32_e32 v83, v91
	global_store_dwordx4 v[60:61], v[68:71], off sc1
	v_pk_add_f32 v[62:63], v[22:23], v[66:67]
	v_pk_add_f32 v[60:61], v[20:21], v[64:65]
	v_pk_add_f32 v[58:59], v[14:15], v[58:59]
	v_pk_add_f32 v[56:57], v[12:13], v[56:57]
	v_cvt_pk_f16_f32 v40, v40, v41
	v_cvt_pk_f16_f32 v41, v42, v43
	v_pk_add_f32 v[46:47], v[14:15], v[46:47]
	v_pk_add_f32 v[42:43], v[12:13], v[44:45]
	v_pk_add_f32 v[34:35], v[10:11], v[34:35]
	v_pk_add_f32 v[32:33], v[8:9], v[32:33]
	v_pk_add_f32 v[26:27], v[6:7], v[26:27]
	v_pk_add_f32 v[24:25], v[4:5], v[24:25]
	v_pk_add_f32 v[22:23], v[22:23], v[38:39]
	v_pk_add_f32 v[20:21], v[20:21], v[36:37]
	v_pk_add_f32 v[14:15], v[14:15], v[30:31]
	v_pk_add_f32 v[12:13], v[12:13], v[28:29]
	v_pk_add_f32 v[10:11], v[10:11], v[18:19]
	v_pk_add_f32 v[8:9], v[8:9], v[16:17]
	v_pk_add_f32 v[2:3], v[6:7], v[2:3]
	v_pk_add_f32 v[0:1], v[4:5], v[0:1]
	v_cvt_pk_f16_f32 v60, v60, v61
	v_cvt_pk_f16_f32 v61, v62, v63
	v_cvt_pk_f16_f32 v62, v56, v57
	v_cvt_pk_f16_f32 v63, v58, v59
	v_lshl_add_u64 v[56:57], v[72:73], 0, v[84:85]
	v_cvt_pk_f16_f32 v42, v42, v43
	v_cvt_pk_f16_f32 v43, v46, v47
	v_lshl_add_u64 v[44:45], v[72:73], 0, v[80:81]
	v_cvt_pk_f16_f32 v32, v32, v33
	v_cvt_pk_f16_f32 v33, v34, v35
	v_cvt_pk_f16_f32 v34, v24, v25
	v_cvt_pk_f16_f32 v35, v26, v27
	v_lshl_add_u64 v[24:25], v[74:75], 0, v[80:81]
	v_cvt_pk_f16_f32 v20, v20, v21
	v_cvt_pk_f16_f32 v21, v22, v23
	v_cvt_pk_f16_f32 v22, v12, v13
	v_cvt_pk_f16_f32 v23, v14, v15
	v_lshl_add_u64 v[12:13], v[72:73], 0, v[82:83]
	v_cvt_pk_f16_f32 v8, v8, v9
	v_cvt_pk_f16_f32 v9, v10, v11
	v_cvt_pk_f16_f32 v10, v0, v1
	v_cvt_pk_f16_f32 v11, v2, v3
	v_lshl_add_u64 v[0:1], v[74:75], 0, v[82:83]
	global_store_dwordx4 v[56:57], v[60:63], off sc1
	global_store_dwordx4 v[44:45], v[40:43], off sc1
	global_store_dwordx4 v[24:25], v[32:35], off sc1
	global_store_dwordx4 v[12:13], v[20:23], off sc1
	global_store_dwordx4 v[0:1], v[8:11], off sc1
	s_waitcnt vmcnt(0)
	s_cmpk_gt_u32 s18, 0xff
	s_cbranch_scc1 .LBB1_10
	s_barrier

.LBB2_3:
	s_mov_b32 s16, s15
	v_add_u32_e32 v116, s16, v87
	v_add_u32_e32 v148, s16, v0
	ds_read_b128 v[88:91], v116 offset:16384
	ds_read_b128 v[92:95], v116 offset:17408
	ds_read_b128 v[96:99], v116 offset:18432
	ds_read_b128 v[100:103], v116 offset:19456
	ds_read_b128 v[104:107], v116 offset:32768
	ds_read_b128 v[108:111], v116 offset:33792
	ds_read_b128 v[112:115], v116 offset:34816
	ds_read_b128 v[116:119], v116 offset:35840
	s_lshl_b32 s15, s7, 7
	s_ashr_i32 s17, s15, 31
	s_add_u32 s18, s4, s15
	s_addc_u32 s19, s5, s17
	s_add_u32 s20, s2, s15
	s_addc_u32 s21, s3, s17
	s_add_i32 s15, s6, s14
	s_add_i32 m0, s15, 0x4000
	s_nop 0
	global_load_lds_dwordx4 v82, s[18:19]
	ds_read_b128 v[120:123], v148
	ds_read_b128 v[124:127], v148 offset:1024
	ds_read_b128 v[128:131], v148 offset:2048
	s_add_i32 m0, s15, 0x6000
	s_nop 0
	global_load_lds_dwordx4 v84, s[18:19]
	ds_read_b128 v[132:135], v148 offset:3072
	ds_read_b128 v[136:139], v148 offset:4096
	ds_read_b128 v[140:143], v148 offset:5120
	s_mov_b32 m0, s15
	s_nop 0
	global_load_lds_dwordx4 v82, s[20:21]
	ds_read_b128 v[144:147], v148 offset:6144
	ds_read_b128 v[148:151], v148 offset:7168
	s_waitcnt vmcnt(3)
	s_waitcnt lgkmcnt(0)
	s_barrier
	s_setprio 1
	s_waitcnt lgkmcnt(0)
	v_mfma_f32_16x16x32_f16 v[18:21], v[88:91], v[120:123], v[18:21]
	s_add_u32 s18, s18, 0x40000
	s_addc_u32 s19, s19, 0
	s_add_i32 m0, s15, 0x8000
	v_mfma_f32_16x16x32_f16 v[70:73], v[96:99], v[120:123], v[70:73]
	global_load_lds_dwordx4 v82, s[18:19]
	s_add_i32 m0, s15, 0xa000
	v_mfma_f32_16x16x32_f16 v[58:61], v[88:91], v[128:131], v[58:61]
	global_load_lds_dwordx4 v84, s[18:19]
	s_add_i32 m0, s15, 0x2000
	v_mfma_f32_16x16x32_f16 v[54:57], v[96:99], v[128:131], v[54:57]
	global_load_lds_dwordx4 v84, s[20:21]
	v_mfma_f32_16x16x32_f16 v[18:21], v[92:95], v[124:127], v[18:21]
	v_mfma_f32_16x16x32_f16 v[70:73], v[100:103], v[124:127], v[70:73]
	v_mfma_f32_16x16x32_f16 v[58:61], v[92:95], v[132:135], v[58:61]
	v_mfma_f32_16x16x32_f16 v[54:57], v[100:103], v[132:135], v[54:57]
	v_mfma_f32_16x16x32_f16 v[42:45], v[88:91], v[136:139], v[42:45]
	v_mfma_f32_16x16x32_f16 v[38:41], v[96:99], v[136:139], v[38:41]
	v_mfma_f32_16x16x32_f16 v[26:29], v[88:91], v[144:147], v[26:29]
	v_mfma_f32_16x16x32_f16 v[22:25], v[96:99], v[144:147], v[22:25]
	v_mfma_f32_16x16x32_f16 v[42:45], v[92:95], v[140:143], v[42:45]
	v_mfma_f32_16x16x32_f16 v[38:41], v[100:103], v[140:143], v[38:41]
	v_mfma_f32_16x16x32_f16 v[26:29], v[92:95], v[148:151], v[26:29]
	v_mfma_f32_16x16x32_f16 v[22:25], v[100:103], v[148:151], v[22:25]
	v_mfma_f32_16x16x32_f16 v[78:81], v[104:107], v[120:123], v[78:81]
	v_mfma_f32_16x16x32_f16 v[74:77], v[112:115], v[120:123], v[74:77]
	v_mfma_f32_16x16x32_f16 v[66:69], v[104:107], v[128:131], v[66:69]
	v_mfma_f32_16x16x32_f16 v[62:65], v[112:115], v[128:131], v[62:65]
	v_mfma_f32_16x16x32_f16 v[78:81], v[108:111], v[124:127], v[78:81]
	v_mfma_f32_16x16x32_f16 v[74:77], v[116:119], v[124:127], v[74:77]
	v_mfma_f32_16x16x32_f16 v[66:69], v[108:111], v[132:135], v[66:69]
	v_mfma_f32_16x16x32_f16 v[62:65], v[116:119], v[132:135], v[62:65]
	v_mfma_f32_16x16x32_f16 v[50:53], v[104:107], v[136:139], v[50:53]
	v_mfma_f32_16x16x32_f16 v[46:49], v[112:115], v[136:139], v[46:49]
	s_add_i32 s7, s7, 1
	s_cmp_lg_u32 s7, 16
	v_mfma_f32_16x16x32_f16 v[34:37], v[104:107], v[144:147], v[34:37]
	s_cselect_b32 s7, s7, 0
	v_mfma_f32_16x16x32_f16 v[30:33], v[112:115], v[144:147], v[30:33]
	s_add_i32 s11, s11, -1
	v_mfma_f32_16x16x32_f16 v[50:53], v[108:111], v[140:143], v[50:53]
	s_mov_b32 s15, s13
	v_mfma_f32_16x16x32_f16 v[46:49], v[116:119], v[140:143], v[46:49]
	s_mov_b32 s13, s14
	v_mfma_f32_16x16x32_f16 v[34:37], v[108:111], v[148:151], v[34:37]
	s_mov_b32 s14, s16
	v_mfma_f32_16x16x32_f16 v[30:33], v[116:119], v[148:151], v[30:33]
	s_cmp_lg_u32 s11, 0
	s_setprio 0
	s_barrier
	s_cbranch_scc1 .LBB2_3
	v_lshl_add_u32 v0, s0, 7, v86
	v_or_b32_e32 v88, s10, v1
	v_ashrrev_i32_e32 v1, 31, v0
	v_lshlrev_b64 v[82:83], 12, v[0:1]
	v_or_b32_e32 v88, s1, v88
	v_lshl_add_u64 v[82:83], s[8:9], 0, v[82:83]
	v_lshlrev_b32_e32 v88, 2, v88
	v_mov_b32_e32 v89, 0
	v_or_b32_e32 v84, 16, v0
	v_lshl_add_u64 v[82:83], v[82:83], 0, v[88:89]
	v_pk_add_f32 v[20:21], v[16:17], v[20:21]
	v_pk_add_f32 v[18:19], v[14:15], v[18:19]
	v_ashrrev_i32_e32 v85, 31, v84
	global_store_dwordx4 v[82:83], v[18:21], off sc1
	v_lshlrev_b64 v[84:85], 12, v[84:85]
	v_lshl_add_u64 v[84:85], s[8:9], 0, v[84:85]
	v_pk_add_f32 v[20:21], v[12:13], v[72:73]
	v_pk_add_f32 v[18:19], v[10:11], v[70:71]
	global_store_dwordx4 v[82:83], v[18:21], off offset:64 sc1
	v_or_b32_e32 v86, 32, v0
	v_lshl_add_u64 v[84:85], v[84:85], 0, v[88:89]
	v_pk_add_f32 v[20:21], v[8:9], v[80:81]
	v_pk_add_f32 v[18:19], v[6:7], v[78:79]
	global_store_dwordx4 v[82:83], v[18:21], off offset:512 sc1
	v_ashrrev_i32_e32 v87, 31, v86
	v_lshlrev_b64 v[86:87], 12, v[86:87]
	v_pk_add_f32 v[20:21], v[4:5], v[76:77]
	v_pk_add_f32 v[18:19], v[2:3], v[74:75]
	global_store_dwordx4 v[82:83], v[18:21], off offset:576 sc1
	v_lshl_add_u64 v[86:87], s[8:9], 0, v[86:87]
	v_or_b32_e32 v0, 48, v0
	v_pk_add_f32 v[20:21], v[16:17], v[60:61]
	v_pk_add_f32 v[18:19], v[14:15], v[58:59]
	global_store_dwordx4 v[84:85], v[18:21], off sc1
	v_ashrrev_i32_e32 v1, 31, v0
	v_lshl_add_u64 v[86:87], v[86:87], 0, v[88:89]
	v_pk_add_f32 v[20:21], v[12:13], v[56:57]
	v_pk_add_f32 v[18:19], v[10:11], v[54:55]
	global_store_dwordx4 v[84:85], v[18:21], off offset:64 sc1
	v_lshlrev_b64 v[0:1], 12, v[0:1]
	v_lshl_add_u64 v[0:1], s[8:9], 0, v[0:1]
	v_pk_add_f32 v[20:21], v[8:9], v[68:69]
	v_pk_add_f32 v[18:19], v[6:7], v[66:67]
	global_store_dwordx4 v[84:85], v[18:21], off offset:512 sc1
	v_lshl_add_u64 v[0:1], v[0:1], 0, v[88:89]
	s_cmpk_gt_u32 s12, 0xff
	v_pk_add_f32 v[20:21], v[4:5], v[64:65]
	v_pk_add_f32 v[18:19], v[2:3], v[62:63]
	global_store_dwordx4 v[84:85], v[18:21], off offset:576 sc1
	s_nop 1
	v_pk_add_f32 v[20:21], v[16:17], v[44:45]
	v_pk_add_f32 v[18:19], v[14:15], v[42:43]
	global_store_dwordx4 v[86:87], v[18:21], off sc1
	v_pk_add_f32 v[16:17], v[16:17], v[28:29]
	v_pk_add_f32 v[14:15], v[14:15], v[26:27]
	v_pk_add_f32 v[20:21], v[12:13], v[40:41]
	v_pk_add_f32 v[18:19], v[10:11], v[38:39]
	global_store_dwordx4 v[86:87], v[18:21], off offset:64 sc1
	v_pk_add_f32 v[12:13], v[12:13], v[24:25]
	v_pk_add_f32 v[10:11], v[10:11], v[22:23]
	v_pk_add_f32 v[20:21], v[8:9], v[52:53]
	v_pk_add_f32 v[18:19], v[6:7], v[50:51]
	global_store_dwordx4 v[86:87], v[18:21], off offset:512 sc1
	v_pk_add_f32 v[8:9], v[8:9], v[36:37]
	v_pk_add_f32 v[6:7], v[6:7], v[34:35]
	v_pk_add_f32 v[20:21], v[4:5], v[48:49]
	v_pk_add_f32 v[18:19], v[2:3], v[46:47]
	v_pk_add_f32 v[4:5], v[4:5], v[32:33]
	v_pk_add_f32 v[2:3], v[2:3], v[30:31]
	global_store_dwordx4 v[86:87], v[18:21], off offset:576 sc1
	global_store_dwordx4 v[0:1], v[14:17], off sc1
	global_store_dwordx4 v[0:1], v[10:13], off offset:64 sc1
	global_store_dwordx4 v[0:1], v[6:9], off offset:512 sc1
	global_store_dwordx4 v[0:1], v[2:5], off offset:576 sc1
	s_waitcnt vmcnt(0)
	s_cbranch_scc1 .LBB2_6
	s_barrier
